# v98 + stage-C work queue reordered too: next layer's weight-transpose units dealt right after the static moba units, before ret_C/ssd_C/lru_C
# baseline (speedup 1.0000x reference)
.LBB0_851:
	s_cmpk_lt_u32 s26, 0x100
	s_cbranch_scc1 .Lqc_done
	v_readlane_b32 s100, v253, 37
	s_nop 0
	s_and_b32 s100, s100, 0x348
	s_add_i32 s101, s100, 0x100
	s_cmp_lt_u32 s26, s101
	s_cbranch_scc0 .Lqc_b
	s_add_i32 s26, s26, 0x300
	s_branch .Lqc_done
.Lqc_b:
	s_add_i32 s101, s101, 0x300
	s_cmp_lt_u32 s26, s101
	s_cbranch_scc0 .Lqc_done
	s_sub_i32 s26, s26, s100
.Lqc_done:
	s_mov_b32 s74, 0
	v_mov_b32_e32 v204, v0
	s_cmpk_gt_i32 s26, 0xff
	s_cbranch_scc0 .LBB0_917
	s_cmpk_gt_u32 s26, 0x1ff
	s_cbranch_scc0 .LBB0_918
	s_cmpk_gt_u32 s26, 0x2ff
	s_cbranch_scc0 .LBB0_919
	s_cmpk_gt_u32 s26, 0x3ff
	s_cbranch_scc0 .LBB0_920
	s_cmpk_lt_u32 s26, 0x748
	v_readlane_b32 s4, v253, 37
	s_cselect_b64 s[0:1], -1, 0
	v_readlane_b32 s5, v253, 38
	s_and_b64 s[4:5], s[4:5], s[0:1]
	s_mov_b64 s[0:1], 0
	s_and_b64 vcc, exec, s[4:5]
	s_mov_b64 s[4:5], 0
	s_cbranch_vccz .LBB0_921
	s_ashr_i32 s75, s74, 31
	s_lshl_b64 s[6:7], s[74:75], 2
	v_readlane_b32 s4, v253, 39
	s_add_u32 s4, s4, s6
	v_readlane_b32 s5, v253, 45
	s_addc_u32 s5, s5, s7
	s_lshl_b32 s10, s26, 1
	s_add_i32 s8, s10, 0xfe90
	s_and_b32 s9, s8, 0xfffe
	s_mulk_i32 s9, 0x4e05
	s_lshr_b32 s11, s9, 21
	s_mulk_i32 s11, 0x69
	s_sub_i32 s8, s8, s11
	s_lshr_b32 s9, s9, 14
	s_lshl_b32 s8, s8, 7
	v_lshlrev_b32_e32 v1, 2, v204
	s_and_b32 s78, s9, 0xff80
	s_and_b32 s14, s8, 0xff80
	v_and_b32_e32 v14, 0x7c, v1
	v_ashrrev_i32_e32 v68, 5, v204
	s_waitcnt lgkmcnt(0)
	v_or_b32_e32 v2, s14, v14
	s_movk_i32 s8, 0x3410
	v_add_u32_e32 v10, s78, v68
	v_readfirstlane_b32 s13, v204
	v_cmp_gt_u32_e32 vcc, s8, v2
	v_ashrrev_i32_e32 v11, 31, v10
	v_mov_b32_e32 v8, 0
	v_lshlrev_b32_e32 v2, 2, v2
	v_mov_b32_e32 v4, 0
	v_mov_b32_e32 v5, 0
	v_mov_b32_e32 v6, 0
	v_mov_b32_e32 v7, 0
	s_and_saveexec_b64 s[8:9], vcc
	s_cbranch_execz .LBB0_858
	v_mov_b64_e32 v[4:5], s[4:5]
	s_mov_b32 s11, 0xd040
	v_mad_i64_i32 v[4:5], s[16:17], v10, s11, v[4:5]
	v_lshl_add_u64 v[4:5], v[4:5], 0, v[2:3]
	global_load_dwordx4 v[4:7], v[4:5], off
